# v25
# speedup vs baseline: 1.0155x; 1.0049x over previous
.LBB2_63:
	v_lshrrev_b32_e32 v69, 5, v68
	v_lshlrev_b32_e32 v90, 8, v75
	v_xor_b32_e32 v2, v69, v73
	v_lshl_or_b32 v84, v2, 4, v90
	s_waitcnt lgkmcnt(0)
	s_barrier
	ds_read_b128 v[2:5], v84
	v_or_b32_e32 v6, 32, v75
	v_min_i32_e32 v75, 59, v6
	v_lshlrev_b32_e32 v91, 8, v75
	v_bitop3_b32 v6, v69, v75, 15 bitop3:0x78
	v_lshl_or_b32 v85, v6, 4, v91
	s_waitcnt vmcnt(7) lgkmcnt(0)
	v_mfma_f32_32x32x16_f16 v[18:33], v[2:5], v[46:49], 0
	ds_read_b128 v[2:5], v85
	v_and_b32_e32 v92, 15, v75
	v_bitop3_b32 v75, v69, v92, 2 bitop3:0x36
	v_lshl_or_b32 v83, v75, 4, v91
	s_mov_b32 s0, 0x9000
	s_waitcnt lgkmcnt(0)
	v_mfma_f32_32x32x16_f16 v[2:17], v[2:5], v[46:49], 0
	v_bitop3_b32 v46, v69, v73, 2 bitop3:0x36
	v_lshl_or_b32 v82, v46, 4, v90
	ds_read_b128 v[46:49], v82
	s_waitcnt vmcnt(6) lgkmcnt(0)
	v_mfma_f32_32x32x16_f16 v[18:33], v[46:49], v[34:37], v[18:33]
	ds_read_b128 v[46:49], v83
	s_waitcnt lgkmcnt(0)
	v_mfma_f32_32x32x16_f16 v[2:17], v[46:49], v[34:37], v[2:17]
	v_bitop3_b32 v34, v69, v73, 4 bitop3:0x36
	v_lshl_or_b32 v81, v34, 4, v90
	ds_read_b128 v[34:37], v81
	v_bitop3_b32 v46, v69, v92, 4 bitop3:0x36
	v_lshl_or_b32 v80, v46, 4, v91
	v_bitop3_b32 v46, v69, v92, 6 bitop3:0x36
	v_lshl_or_b32 v79, v46, 4, v91
	s_waitcnt vmcnt(5) lgkmcnt(0)
	v_mfma_f32_32x32x16_f16 v[18:33], v[34:37], v[54:57], v[18:33]
	ds_read_b128 v[34:37], v80
	v_bitop3_b32 v46, v69, v73, 8 bitop3:0x36
	v_lshl_or_b32 v76, v46, 4, v90
	ds_read_b128 v[46:49], v76
	s_waitcnt lgkmcnt(1)
	v_mfma_f32_32x32x16_f16 v[2:17], v[34:37], v[54:57], v[2:17]
	v_bitop3_b32 v34, v69, v73, 6 bitop3:0x36
	v_lshl_or_b32 v78, v34, 4, v90
	ds_read_b128 v[34:37], v78
	s_waitcnt vmcnt(4) lgkmcnt(0)
	v_mfma_f32_32x32x16_f16 v[18:33], v[34:37], v[38:41], v[18:33]
	ds_read_b128 v[34:37], v79
	s_waitcnt lgkmcnt(0)
	v_mfma_f32_32x32x16_f16 v[2:17], v[34:37], v[38:41], v[2:17]
	v_add_co_u32_e32 v38, vcc, s0, v70
	v_bitop3_b32 v34, v69, v92, 8 bitop3:0x36
	s_nop 0
	v_addc_co_u32_e32 v39, vcc, 0, v71, vcc
	global_load_dwordx4 v[54:57], v[38:39], off offset:-4096
	v_lshl_or_b32 v77, v34, 4, v91
	ds_read_b128 v[34:37], v77
	v_bitop3_b32 v40, v69, v73, 10 bitop3:0x36
	v_lshl_or_b32 v75, v40, 4, v90
	s_waitcnt vmcnt(4) lgkmcnt(0)
	v_mfma_f32_32x32x16_f16 v[2:17], v[34:37], v[62:65], v[2:17]
	ds_read_b128 v[34:37], v75
	s_mov_b32 s0, 0xb000
	v_mfma_f32_32x32x16_f16 v[18:33], v[46:49], v[62:65], v[18:33]
	global_load_dwordx4 v[46:49], v[38:39], off
	v_bitop3_b32 v38, v69, v92, 10 bitop3:0x36
	v_lshl_or_b32 v63, v38, 4, v91
	v_add_co_u32_e32 v64, vcc, s0, v70
	v_bitop3_b32 v38, v69, v73, 12 bitop3:0x36
	s_nop 0
	v_addc_co_u32_e32 v65, vcc, 0, v71, vcc
	s_waitcnt vmcnt(4) lgkmcnt(0)
	v_mfma_f32_32x32x16_f16 v[18:33], v[34:37], v[42:45], v[18:33]
	ds_read_b128 v[34:37], v63
	v_lshl_or_b32 v62, v38, 4, v90
	global_load_dwordx4 v[38:41], v[64:65], off offset:-4096
	ds_read_b128 v[86:89], v62
	s_mov_b32 s0, 0xd000
	s_waitcnt lgkmcnt(1)
	v_mfma_f32_32x32x16_f16 v[2:17], v[34:37], v[42:45], v[2:17]
	v_bitop3_b32 v34, v69, v92, 12 bitop3:0x36
	v_lshl_or_b32 v44, v34, 4, v91
	ds_read_b128 v[34:37], v44
	v_bitop3_b32 v42, v69, v73, 14 bitop3:0x36
	v_lshl_or_b32 v42, v42, 4, v90
	v_bitop3_b32 v43, v69, v92, 14 bitop3:0x36
	v_lshl_or_b32 v43, v43, 4, v91
	s_waitcnt vmcnt(4) lgkmcnt(1)
	v_mfma_f32_32x32x16_f16 v[18:33], v[86:89], v[58:61], v[18:33]
	s_waitcnt lgkmcnt(0)
	v_mfma_f32_32x32x16_f16 v[2:17], v[34:37], v[58:61], v[2:17]
	ds_read_b128 v[58:61], v42
	global_load_dwordx4 v[34:37], v[64:65], off
	v_add_co_u32_e32 v64, vcc, s0, v70
	s_mov_b32 s0, 0xf000
	s_nop 0
	v_addc_co_u32_e32 v65, vcc, 0, v71, vcc
	s_waitcnt vmcnt(4) lgkmcnt(0)
	v_mfma_f32_32x32x16_f16 v[18:33], v[58:61], v[50:53], v[18:33]
	ds_read_b128 v[58:61], v43
	s_waitcnt lgkmcnt(0)
	v_mfma_f32_32x32x16_f16 v[2:17], v[58:61], v[50:53], v[2:17]
	ds_read_b128 v[50:53], v84 offset:15360
	global_load_dwordx4 v[58:61], v[64:65], off offset:-4096
	s_waitcnt vmcnt(4) lgkmcnt(0)
	v_mfma_f32_32x32x16_f16 v[18:33], v[50:53], v[54:57], v[18:33]
	ds_read_b128 v[50:53], v85 offset:15360
	s_waitcnt lgkmcnt(0)
	v_mfma_f32_32x32x16_f16 v[2:17], v[50:53], v[54:57], v[2:17]
	ds_read_b128 v[50:53], v82 offset:15360
	global_load_dwordx4 v[54:57], v[64:65], off
	v_add_co_u32_e32 v64, vcc, s0, v70
	s_movk_i32 s0, 0x440
	s_nop 0
	v_addc_co_u32_e32 v65, vcc, 0, v71, vcc
	s_waitcnt vmcnt(4) lgkmcnt(0)
	v_mfma_f32_32x32x16_f16 v[18:33], v[50:53], v[46:49], v[18:33]
	ds_read_b128 v[50:53], v83 offset:15360
	v_cmp_gt_u32_e32 vcc, 32, v68
	s_waitcnt lgkmcnt(0)
	v_mfma_f32_32x32x16_f16 v[2:17], v[50:53], v[46:49], v[2:17]
	ds_read_b128 v[46:49], v81 offset:15360
	global_load_dwordx4 v[50:53], v[64:65], off offset:-4096
	s_waitcnt vmcnt(4) lgkmcnt(0)
	v_mfma_f32_32x32x16_f16 v[18:33], v[46:49], v[38:41], v[18:33]
	ds_read_b128 v[46:49], v80 offset:15360
	s_waitcnt lgkmcnt(0)
	v_mfma_f32_32x32x16_f16 v[2:17], v[46:49], v[38:41], v[2:17]
	ds_read_b128 v[46:49], v78 offset:15360
	global_load_dwordx4 v[38:41], v[64:65], off
	s_waitcnt vmcnt(4) lgkmcnt(0)
	v_mfma_f32_32x32x16_f16 v[18:33], v[46:49], v[34:37], v[18:33]
	ds_read_b128 v[46:49], v79 offset:15360
	s_waitcnt lgkmcnt(0)
	v_mfma_f32_32x32x16_f16 v[2:17], v[46:49], v[34:37], v[2:17]
	ds_read_b128 v[34:37], v76 offset:15360
	s_waitcnt vmcnt(3) lgkmcnt(0)
	v_mfma_f32_32x32x16_f16 v[18:33], v[34:37], v[58:61], v[18:33]
	ds_read_b128 v[34:37], v77 offset:15360
	s_waitcnt lgkmcnt(0)
	v_mfma_f32_32x32x16_f16 v[2:17], v[34:37], v[58:61], v[2:17]
	ds_read_b128 v[34:37], v75 offset:15360
	s_waitcnt vmcnt(2) lgkmcnt(0)
	v_mfma_f32_32x32x16_f16 v[18:33], v[34:37], v[54:57], v[18:33]
	ds_read_b128 v[34:37], v63 offset:15360
	s_waitcnt lgkmcnt(0)
	v_mfma_f32_32x32x16_f16 v[2:17], v[34:37], v[54:57], v[2:17]
	ds_read_b128 v[34:37], v62 offset:15360
	s_waitcnt vmcnt(1) lgkmcnt(0)
	v_mfma_f32_32x32x16_f16 v[18:33], v[34:37], v[50:53], v[18:33]
	ds_read_b128 v[34:37], v44 offset:15360
	s_waitcnt lgkmcnt(0)
	v_mfma_f32_32x32x16_f16 v[2:17], v[34:37], v[50:53], v[2:17]
	ds_read_b128 v[44:47], v42 offset:15360
	ds_read_b128 v[48:51], v43 offset:15360
	v_lshlrev_b32_e32 v34, 1, v74
	v_mad_u32_u24 v36, v69, s0, v34
	s_waitcnt lgkmcnt(0)
	s_barrier
	s_waitcnt vmcnt(0)
	v_mfma_f32_32x32x16_f16 v[18:33], v[44:47], v[38:41], v[18:33]
	v_mfma_f32_32x32x16_f16 v[2:17], v[48:51], v[38:41], v[2:17]
	s_setprio 0
	s_nop 9
	v_add_f32_e32 v18, v67, v18
	v_max_f32_e32 v18, 0, v18
	v_add_f32_e32 v19, v67, v19
	v_cvt_f16_f32_e32 v35, v18
	v_max_f32_e32 v19, 0, v19
	v_cvt_f16_f32_e32 v19, v19
	v_add_f32_e32 v20, v67, v20
	v_add_f32_e32 v2, v67, v2
	v_max_f32_e32 v2, 0, v2
	v_cvt_f16_f32_e32 v2, v2
	v_add_f32_e32 v3, v67, v3
	v_max_f32_e32 v3, 0, v3
	v_cvt_f16_f32_e32 v3, v3
	v_max_f32_e32 v20, 0, v20
	v_cvt_f16_f32_e32 v20, v20
	ds_write_b16 v36, v35
	ds_write_b16 v36, v2 offset:8704
	ds_write_b16 v36, v19 offset:272
	ds_write_b16 v36, v3 offset:8976
	ds_write_b16 v36, v20 offset:544
	v_add_f32_e32 v2, v67, v4
	v_max_f32_e32 v2, 0, v2
	v_add_f32_e32 v3, v67, v21
	v_cvt_f16_f32_e32 v2, v2
	v_max_f32_e32 v3, 0, v3
	v_add_f32_e32 v4, v67, v5
	v_cvt_f16_f32_e32 v3, v3
	v_max_f32_e32 v4, 0, v4
	v_add_f32_e32 v5, v67, v22
	v_cvt_f16_f32_e32 v4, v4
	v_max_f32_e32 v5, 0, v5
	v_cvt_f16_f32_e32 v5, v5
	ds_write_b16 v36, v2 offset:9248
	ds_write_b16 v36, v3 offset:816
	ds_write_b16 v36, v4 offset:9520
	ds_write_b16 v36, v5 offset:2176
	v_add_f32_e32 v2, v67, v6
	v_max_f32_e32 v2, 0, v2
	v_add_f32_e32 v3, v67, v23
	v_cvt_f16_f32_e32 v2, v2
	v_max_f32_e32 v3, 0, v3
	v_add_f32_e32 v4, v67, v7
	v_cvt_f16_f32_e32 v3, v3
	v_max_f32_e32 v4, 0, v4
	v_add_f32_e32 v5, v67, v24
	v_cvt_f16_f32_e32 v4, v4
	v_max_f32_e32 v5, 0, v5
	v_cvt_f16_f32_e32 v5, v5
	ds_write_b16 v36, v2 offset:10880
	ds_write_b16 v36, v3 offset:2448
	ds_write_b16 v36, v4 offset:11152
	ds_write_b16 v36, v5 offset:2720
	v_add_f32_e32 v2, v67, v8
	v_max_f32_e32 v2, 0, v2
	v_add_f32_e32 v3, v67, v25
	v_cvt_f16_f32_e32 v2, v2
	v_max_f32_e32 v3, 0, v3
	v_add_f32_e32 v4, v67, v9
	v_cvt_f16_f32_e32 v3, v3
	v_max_f32_e32 v4, 0, v4
	v_add_f32_e32 v5, v67, v26
	v_cvt_f16_f32_e32 v4, v4
	v_max_f32_e32 v5, 0, v5
	v_cvt_f16_f32_e32 v5, v5
	ds_write_b16 v36, v2 offset:11424
	ds_write_b16 v36, v3 offset:2992
	ds_write_b16 v36, v4 offset:11696
	ds_write_b16 v36, v5 offset:4352
	v_add_f32_e32 v2, v67, v10
	v_max_f32_e32 v2, 0, v2
	v_add_f32_e32 v3, v67, v27
	v_cvt_f16_f32_e32 v2, v2
	v_max_f32_e32 v3, 0, v3
	v_add_f32_e32 v4, v67, v11
	v_cvt_f16_f32_e32 v3, v3
	v_max_f32_e32 v4, 0, v4
	v_add_f32_e32 v5, v67, v28
	v_cvt_f16_f32_e32 v4, v4
	v_max_f32_e32 v5, 0, v5
	v_cvt_f16_f32_e32 v5, v5
	ds_write_b16 v36, v2 offset:13056
	ds_write_b16 v36, v3 offset:4624
	ds_write_b16 v36, v4 offset:13328
	ds_write_b16 v36, v5 offset:4896
	v_add_f32_e32 v2, v67, v12
	v_max_f32_e32 v2, 0, v2
	v_add_f32_e32 v3, v67, v29
	v_cvt_f16_f32_e32 v2, v2
	v_max_f32_e32 v3, 0, v3
	v_add_f32_e32 v4, v67, v13
	v_cvt_f16_f32_e32 v3, v3
	v_max_f32_e32 v4, 0, v4
	v_add_f32_e32 v5, v67, v30
	v_cvt_f16_f32_e32 v4, v4
	v_max_f32_e32 v5, 0, v5
	v_mul_u32_u24_e32 v18, 0x440, v69
	v_cvt_f16_f32_e32 v5, v5
	ds_write_b16 v36, v2 offset:13600
	ds_write_b16 v36, v3 offset:5168
	ds_write_b16 v36, v4 offset:13872
	ds_write_b16 v36, v5 offset:6528
	s_and_saveexec_b64 s[0:1], vcc
	s_cbranch_execz .LBB2_65
	v_add_f32_e32 v2, v67, v14
	v_max_f32_e32 v2, 0, v2
	v_cvt_f16_f32_e32 v2, v2
	ds_write_b16 v34, v2 offset:15232

.LBB2_107:
	s_or_b64 exec, exec, s[2:3]
	s_load_dwordx4 s[4:7], s[0:1], 0x38
	s_cmpk_lt_i32 s19, 0x181
	s_cbranch_scc0 .LBB2_62
	s_branch .LBB2_63
	s_nop 0
	s_nop 0
	s_nop 0
	s_nop 0
	s_nop 0
	s_nop 0
	s_nop 0
	s_nop 0
	s_nop 0
	s_endpgm

.LBB3_61:
	v_lshrrev_b32_e32 v67, 5, v66
	v_lshlrev_b32_e32 v88, 8, v72
	s_waitcnt vmcnt(8)
	v_xor_b32_e32 v2, v67, v71
	v_lshl_or_b32 v80, v2, 4, v88
	s_waitcnt lgkmcnt(0)
	s_barrier
	ds_read_b128 v[2:5], v80
	v_or_b32_e32 v6, 32, v72
	v_min_i32_e32 v72, 59, v6
	v_lshlrev_b32_e32 v89, 8, v72
	v_bitop3_b32 v6, v67, v72, 15 bitop3:0x78
	v_lshl_or_b32 v81, v6, 4, v89
	s_waitcnt vmcnt(7) lgkmcnt(0)
	v_mfma_f32_32x32x16_f16 v[18:33], v[2:5], v[46:49], 0
	ds_read_b128 v[2:5], v81
	v_and_b32_e32 v90, 15, v72
	v_bitop3_b32 v72, v67, v90, 2 bitop3:0x36
	v_lshl_or_b32 v79, v72, 4, v89
	s_mov_b32 s0, 0x9000
	s_waitcnt lgkmcnt(0)
	v_mfma_f32_32x32x16_f16 v[2:17], v[2:5], v[46:49], 0
	v_bitop3_b32 v46, v67, v71, 2 bitop3:0x36
	v_lshl_or_b32 v78, v46, 4, v88
	ds_read_b128 v[46:49], v78
	s_waitcnt vmcnt(6) lgkmcnt(0)
	v_mfma_f32_32x32x16_f16 v[18:33], v[46:49], v[34:37], v[18:33]
	ds_read_b128 v[46:49], v79
	s_waitcnt lgkmcnt(0)
	v_mfma_f32_32x32x16_f16 v[2:17], v[46:49], v[34:37], v[2:17]
	v_bitop3_b32 v34, v67, v71, 4 bitop3:0x36
	v_lshl_or_b32 v77, v34, 4, v88
	ds_read_b128 v[34:37], v77
	v_bitop3_b32 v46, v67, v90, 4 bitop3:0x36
	v_lshl_or_b32 v76, v46, 4, v89
	v_bitop3_b32 v46, v67, v90, 6 bitop3:0x36
	v_lshl_or_b32 v75, v46, 4, v89
	s_waitcnt vmcnt(5) lgkmcnt(0)
	v_mfma_f32_32x32x16_f16 v[18:33], v[34:37], v[54:57], v[18:33]
	ds_read_b128 v[34:37], v76
	v_bitop3_b32 v46, v67, v71, 8 bitop3:0x36
	v_lshl_or_b32 v72, v46, 4, v88
	s_waitcnt lgkmcnt(0)
	v_mfma_f32_32x32x16_f16 v[2:17], v[34:37], v[54:57], v[2:17]
	v_bitop3_b32 v34, v67, v71, 6 bitop3:0x36
	v_lshl_or_b32 v74, v34, 4, v88
	ds_read_b128 v[34:37], v74
	ds_read_b128 v[54:57], v72
	s_waitcnt vmcnt(4) lgkmcnt(1)
	v_mfma_f32_32x32x16_f16 v[18:33], v[34:37], v[38:41], v[18:33]
	ds_read_b128 v[34:37], v75
	s_waitcnt lgkmcnt(0)
	v_mfma_f32_32x32x16_f16 v[2:17], v[34:37], v[38:41], v[2:17]
	v_bitop3_b32 v34, v67, v90, 8 bitop3:0x36
	v_lshl_or_b32 v73, v34, 4, v89
	ds_read_b128 v[34:37], v73
	v_add_co_u32_e32 v38, vcc, s0, v68
	s_mov_b32 s0, 0xb000
	s_nop 0
	v_addc_co_u32_e32 v39, vcc, 0, v69, vcc
	s_waitcnt vmcnt(3) lgkmcnt(0)
	v_mfma_f32_32x32x16_f16 v[2:17], v[34:37], v[58:61], v[2:17]
	v_bitop3_b32 v34, v67, v71, 10 bitop3:0x36
	global_load_dwordx4 v[46:49], v[38:39], off offset:-4096
	v_add_co_u32_e32 v86, vcc, s0, v68
	s_mov_b32 s0, 0xd000
	s_nop 0
	v_addc_co_u32_e32 v87, vcc, 0, v69, vcc
	v_mfma_f32_32x32x16_f16 v[18:33], v[54:57], v[58:61], v[18:33]
	v_lshl_or_b32 v58, v34, 4, v88
	ds_read_b128 v[34:37], v58
	v_bitop3_b32 v54, v67, v90, 10 bitop3:0x36
	v_lshl_or_b32 v59, v54, 4, v89
	v_bitop3_b32 v54, v67, v71, 12 bitop3:0x36
	v_lshl_or_b32 v56, v54, 4, v88
	ds_read_b128 v[82:85], v56
	s_waitcnt vmcnt(3) lgkmcnt(1)
	v_mfma_f32_32x32x16_f16 v[18:33], v[34:37], v[42:45], v[18:33]
	ds_read_b128 v[34:37], v59
	v_bitop3_b32 v54, v67, v90, 14 bitop3:0x36
	v_lshl_or_b32 v54, v54, 4, v89
	s_waitcnt lgkmcnt(0)
	v_mfma_f32_32x32x16_f16 v[2:17], v[34:37], v[42:45], v[2:17]
	v_bitop3_b32 v34, v67, v90, 12 bitop3:0x36
	v_lshl_or_b32 v57, v34, 4, v89
	ds_read_b128 v[34:37], v57
	global_load_dwordx4 v[42:45], v[86:87], off offset:-4096
	s_waitcnt vmcnt(3) lgkmcnt(0)
	v_mfma_f32_32x32x16_f16 v[2:17], v[34:37], v[62:65], v[2:17]
	v_bitop3_b32 v34, v67, v71, 14 bitop3:0x36
	v_lshl_or_b32 v55, v34, 4, v88
	global_load_dwordx4 v[34:37], v[86:87], off
	v_mfma_f32_32x32x16_f16 v[18:33], v[82:85], v[62:65], v[18:33]
	ds_read_b128 v[60:63], v55
	v_add_co_u32_e32 v64, vcc, s0, v68
	s_mov_b32 s0, 0xf000
	s_nop 0
	v_addc_co_u32_e32 v65, vcc, 0, v69, vcc
	s_waitcnt vmcnt(3) lgkmcnt(0)
	v_mfma_f32_32x32x16_f16 v[18:33], v[60:63], v[50:53], v[18:33]
	ds_read_b128 v[60:63], v54
	s_waitcnt lgkmcnt(0)
	v_mfma_f32_32x32x16_f16 v[2:17], v[60:63], v[50:53], v[2:17]
	global_load_dwordx4 v[60:63], v[64:65], off offset:-4096
	ds_read_b128 v[50:53], v80 offset:15360
	global_load_dwordx4 v[38:41], v[38:39], off
	s_waitcnt vmcnt(4) lgkmcnt(0)
	v_mfma_f32_32x32x16_f16 v[18:33], v[50:53], v[46:49], v[18:33]
	ds_read_b128 v[50:53], v81 offset:15360
	s_waitcnt lgkmcnt(0)
	v_mfma_f32_32x32x16_f16 v[2:17], v[50:53], v[46:49], v[2:17]
	ds_read_b128 v[46:49], v78 offset:15360
	global_load_dwordx4 v[50:53], v[64:65], off
	v_add_co_u32_e32 v64, vcc, s0, v68
	s_nop 1
	v_addc_co_u32_e32 v65, vcc, 0, v69, vcc
	v_cmp_gt_u32_e32 vcc, 32, v66
	s_waitcnt vmcnt(1) lgkmcnt(0)
	v_mfma_f32_32x32x16_f16 v[18:33], v[46:49], v[38:41], v[18:33]
	ds_read_b128 v[46:49], v79 offset:15360
	s_waitcnt lgkmcnt(0)
	v_mfma_f32_32x32x16_f16 v[2:17], v[46:49], v[38:41], v[2:17]
	ds_read_b128 v[38:41], v77 offset:15360
	global_load_dwordx4 v[46:49], v[64:65], off offset:-4096
	s_waitcnt lgkmcnt(0)
	v_mfma_f32_32x32x16_f16 v[18:33], v[38:41], v[42:45], v[18:33]
	ds_read_b128 v[38:41], v76 offset:15360
	s_waitcnt lgkmcnt(0)
	v_mfma_f32_32x32x16_f16 v[2:17], v[38:41], v[42:45], v[2:17]
	ds_read_b128 v[42:45], v74 offset:15360
	global_load_dwordx4 v[38:41], v[64:65], off
	s_waitcnt lgkmcnt(0)
	v_mfma_f32_32x32x16_f16 v[18:33], v[42:45], v[34:37], v[18:33]
	ds_read_b128 v[42:45], v75 offset:15360
	s_waitcnt lgkmcnt(0)
	v_mfma_f32_32x32x16_f16 v[2:17], v[42:45], v[34:37], v[2:17]
	ds_read_b128 v[34:37], v72 offset:15360
	s_waitcnt lgkmcnt(0)
	v_mfma_f32_32x32x16_f16 v[18:33], v[34:37], v[60:63], v[18:33]
	ds_read_b128 v[34:37], v73 offset:15360
	s_waitcnt lgkmcnt(0)
	v_mfma_f32_32x32x16_f16 v[2:17], v[34:37], v[60:63], v[2:17]
	ds_read_b128 v[34:37], v58 offset:15360
	s_waitcnt vmcnt(2) lgkmcnt(0)
	v_mfma_f32_32x32x16_f16 v[18:33], v[34:37], v[50:53], v[18:33]
	ds_read_b128 v[34:37], v59 offset:15360
	s_waitcnt lgkmcnt(0)
	v_mfma_f32_32x32x16_f16 v[2:17], v[34:37], v[50:53], v[2:17]
	ds_read_b128 v[34:37], v56 offset:15360
	s_waitcnt vmcnt(1) lgkmcnt(0)
	v_mfma_f32_32x32x16_f16 v[18:33], v[34:37], v[46:49], v[18:33]
	ds_read_b128 v[34:37], v57 offset:15360
	s_waitcnt lgkmcnt(0)
	v_mfma_f32_32x32x16_f16 v[2:17], v[34:37], v[46:49], v[2:17]
	ds_read_b128 v[34:37], v55 offset:15360
	s_waitcnt vmcnt(0) lgkmcnt(0)
	v_mfma_f32_32x32x16_f16 v[18:33], v[34:37], v[38:41], v[18:33]
	ds_read_b128 v[34:37], v54 offset:15360
	s_waitcnt lgkmcnt(0)
	s_barrier
	s_setprio 0
	s_nop 7
	v_add_f32_e32 v42, v70, v18
	v_mfma_f32_32x32x16_f16 v[2:17], v[34:37], v[38:41], v[2:17]
	v_lshlrev_b32_e32 v18, 11, v67
	v_or_b32_e32 v43, v1, v18
	v_add_f32_e32 v19, v70, v19
	ds_write2st64_b32 v43, v42, v19 offset1:2
	v_add_f32_e32 v19, v70, v20
	s_nop 6
	v_add_f32_e32 v3, v70, v3
	v_add_f32_e32 v4, v70, v4
	ds_write2st64_b32 v43, v3, v4 offset0:66 offset1:68
	v_add_f32_e32 v3, v70, v21
	ds_write2st64_b32 v43, v19, v3 offset0:4 offset1:6
	v_add_f32_e32 v3, v70, v5
	v_add_f32_e32 v5, v70, v6
	v_add_f32_e32 v4, v70, v22
	ds_write2st64_b32 v43, v3, v5 offset0:70 offset1:80
	v_add_f32_e32 v3, v70, v23
	ds_write2st64_b32 v43, v4, v3 offset0:16 offset1:18
	v_add_f32_e32 v3, v70, v7
	v_add_f32_e32 v5, v70, v8
	v_add_f32_e32 v4, v70, v24
	ds_write2st64_b32 v43, v3, v5 offset0:82 offset1:84
	v_add_f32_e32 v3, v70, v25
	ds_write2st64_b32 v43, v4, v3 offset0:20 offset1:22
	v_add_f32_e32 v3, v70, v9
	v_add_f32_e32 v5, v70, v10
	v_add_f32_e32 v4, v70, v26
	ds_write2st64_b32 v43, v3, v5 offset0:86 offset1:96
	v_add_f32_e32 v3, v70, v27
	ds_write2st64_b32 v43, v4, v3 offset0:32 offset1:34
	v_add_f32_e32 v3, v70, v11
	v_add_f32_e32 v5, v70, v12
	v_add_f32_e32 v4, v70, v28
	ds_write2st64_b32 v43, v3, v5 offset0:98 offset1:100
	v_add_f32_e32 v3, v70, v29
	ds_write2st64_b32 v43, v4, v3 offset0:36 offset1:38
	v_add_f32_e32 v3, v70, v13
	v_add_f32_e32 v2, v70, v2
	ds_write_b32 v43, v3 offset:26112
	v_add_f32_e32 v3, v70, v30
	ds_write2st64_b32 v43, v3, v2 offset0:48 offset1:64
	s_and_saveexec_b64 s[0:1], vcc
	v_add_f32_e32 v2, v70, v14
	ds_write_b32 v1, v2 offset:28672
	s_or_b64 exec, exec, s[0:1]
	v_lshlrev_b32_e32 v3, 2, v67
	v_add_f32_e32 v4, v70, v31
	v_add_u32_e32 v2, v1, v18
	ds_write_b32 v2, v4 offset:12800
	v_or_b32_e32 v4, 57, v3
	v_cmp_gt_u32_e64 s[0:1], 60, v4
	s_and_saveexec_b64 s[4:5], s[0:1]
	v_lshl_or_b32 v4, v4, 9, v1
	v_add_f32_e32 v5, v70, v15
	ds_write_b32 v4, v5
	s_or_b64 exec, exec, s[4:5]
	v_or_b32_e32 v3, 58, v3
	v_add_f32_e32 v4, v70, v32
	v_cmp_gt_u32_e64 s[0:1], 60, v3
	ds_write_b32 v2, v4 offset:13312
	s_and_saveexec_b64 s[4:5], s[0:1]
	v_lshl_or_b32 v3, v3, 9, v1
	v_add_f32_e32 v4, v70, v16
	ds_write_b32 v3, v4
	s_or_b64 exec, exec, s[4:5]
	v_add_f32_e32 v3, v70, v33
	ds_write_b32 v2, v3 offset:13824
	s_and_saveexec_b64 s[0:1], vcc
	v_add_f32_e32 v2, v70, v17
	ds_write_b32 v1, v2 offset:30208
	s_or_b64 exec, exec, s[0:1]
	v_lshlrev_b32_e32 v1, 4, v0
	v_and_b32_e32 v4, 0x1f0, v1
	v_mov_b32_e32 v5, 0
	v_lshrrev_b32_e32 v1, 5, v0
	v_lshl_add_u64 v[2:3], s[2:3], 0, v[4:5]
	v_add_u32_e32 v6, s16, v1
	s_mov_b32 s2, 0x186a0
	v_cmp_gt_i32_e32 vcc, s2, v6
	s_waitcnt lgkmcnt(0)
	s_barrier
	s_and_saveexec_b64 s[0:1], vcc
	s_cbranch_execz .LBB3_71
	v_lshl_or_b32 v1, v1, 9, v4
	ds_read_b128 v[8:11], v1
	v_ashrrev_i32_e32 v7, 31, v6
	v_lshlrev_b64 v[6:7], 9, v[6:7]
	v_lshl_add_u64 v[6:7], v[2:3], 0, v[6:7]
	s_waitcnt lgkmcnt(0)
	global_store_dwordx4 v[6:7], v[8:11], off sc1
